# plus prologue silu table: 18 conditioning loads per thread requested together instead of one dependent round trip each
# baseline (speedup 1.0000x reference)
.LBB0_15:
	s_and_saveexec_b64 s[10:11], s[6:7]
	s_cbranch_execz .LBB0_22
	s_load_dwordx2 s[14:15], s[0:1], 0x8
	s_load_dwordx2 s[16:17], s[0:1], 0x18
	v_mov_b32_e32 v6, v39
	v_mov_b32_e32 v2, v39
	s_waitcnt lgkmcnt(0)
	global_load_dword v163, v2, s[14:15]
	v_add_u32_e32 v2, 0x800, v2
	global_load_dword v164, v2, s[14:15]
	v_add_u32_e32 v2, 0x800, v2
	global_load_dword v165, v2, s[14:15]
	v_add_u32_e32 v2, 0x800, v2
	global_load_dword v166, v2, s[14:15]
	v_add_u32_e32 v2, 0x800, v2
	global_load_dword v167, v2, s[14:15]
	v_add_u32_e32 v2, 0x800, v2
	global_load_dword v168, v2, s[14:15]
	v_add_u32_e32 v2, 0x800, v2
	global_load_dword v169, v2, s[14:15]
	v_add_u32_e32 v2, 0x800, v2
	global_load_dword v170, v2, s[14:15]
	v_add_u32_e32 v2, 0x800, v2
	global_load_dword v171, v2, s[14:15]
	v_add_u32_e32 v2, 0x800, v2
	global_load_dword v172, v2, s[14:15]
	v_add_u32_e32 v2, 0x800, v2
	global_load_dword v173, v2, s[14:15]
	v_add_u32_e32 v2, 0x800, v2
	global_load_dword v174, v2, s[14:15]
	v_add_u32_e32 v2, 0x800, v2
	global_load_dword v175, v2, s[14:15]
	v_add_u32_e32 v2, 0x800, v2
	global_load_dword v176, v2, s[14:15]
	v_add_u32_e32 v2, 0x800, v2
	global_load_dword v177, v2, s[14:15]
	v_add_u32_e32 v2, 0x800, v2
	global_load_dword v178, v2, s[14:15]
	global_load_dword v179, v39, s[16:17]
	v_add_u32_e32 v2, 0x800, v39
	global_load_dword v180, v2, s[16:17]
	s_waitcnt vmcnt(17)
	v_mov_b32_e32 v4, v163
	v_mul_f32_e32 v5, 0xbfb8aa3b, v4
	v_exp_f32_e32 v5, v5
	s_nop 0
	v_add_f32_e32 v5, 1.0, v5
	v_div_scale_f32 v7, s[38:39], v5, v5, v4
	v_rcp_f32_e32 v9, v7
	v_div_scale_f32 v10, vcc, v4, v5, v4
	v_fma_f32 v11, -v7, v9, 1.0
	v_fmac_f32_e32 v9, v11, v9
	v_mul_f32_e32 v11, v10, v9
	v_fma_f32 v12, -v7, v11, v10
	v_fmac_f32_e32 v11, v12, v9
	v_fma_f32 v7, -v7, v11, v10
	v_div_fmas_f32 v7, v7, v9, v11
	v_div_fixup_f32 v4, v7, v5, v4
	ds_write_b32 v6, v4
	v_add_u32_e32 v6, 0x800, v6
	s_waitcnt vmcnt(16)
	v_mov_b32_e32 v4, v164
	v_mul_f32_e32 v5, 0xbfb8aa3b, v4
	v_exp_f32_e32 v5, v5
	s_nop 0
	v_add_f32_e32 v5, 1.0, v5
	v_div_scale_f32 v7, s[38:39], v5, v5, v4
	v_rcp_f32_e32 v9, v7
	v_div_scale_f32 v10, vcc, v4, v5, v4
	v_fma_f32 v11, -v7, v9, 1.0
	v_fmac_f32_e32 v9, v11, v9
	v_mul_f32_e32 v11, v10, v9
	v_fma_f32 v12, -v7, v11, v10
	v_fmac_f32_e32 v11, v12, v9
	v_fma_f32 v7, -v7, v11, v10
	v_div_fmas_f32 v7, v7, v9, v11
	v_div_fixup_f32 v4, v7, v5, v4
	ds_write_b32 v6, v4
	v_add_u32_e32 v6, 0x800, v6
	s_waitcnt vmcnt(15)
	v_mov_b32_e32 v4, v165
	v_mul_f32_e32 v5, 0xbfb8aa3b, v4
	v_exp_f32_e32 v5, v5
	s_nop 0
	v_add_f32_e32 v5, 1.0, v5
	v_div_scale_f32 v7, s[38:39], v5, v5, v4
	v_rcp_f32_e32 v9, v7
	v_div_scale_f32 v10, vcc, v4, v5, v4
	v_fma_f32 v11, -v7, v9, 1.0
	v_fmac_f32_e32 v9, v11, v9
	v_mul_f32_e32 v11, v10, v9
	v_fma_f32 v12, -v7, v11, v10
	v_fmac_f32_e32 v11, v12, v9
	v_fma_f32 v7, -v7, v11, v10
	v_div_fmas_f32 v7, v7, v9, v11
	v_div_fixup_f32 v4, v7, v5, v4
	ds_write_b32 v6, v4
	v_add_u32_e32 v6, 0x800, v6
	s_waitcnt vmcnt(14)
	v_mov_b32_e32 v4, v166
	v_mul_f32_e32 v5, 0xbfb8aa3b, v4
	v_exp_f32_e32 v5, v5
	s_nop 0
	v_add_f32_e32 v5, 1.0, v5
	v_div_scale_f32 v7, s[38:39], v5, v5, v4
	v_rcp_f32_e32 v9, v7
	v_div_scale_f32 v10, vcc, v4, v5, v4
	v_fma_f32 v11, -v7, v9, 1.0
	v_fmac_f32_e32 v9, v11, v9
	v_mul_f32_e32 v11, v10, v9
	v_fma_f32 v12, -v7, v11, v10
	v_fmac_f32_e32 v11, v12, v9
	v_fma_f32 v7, -v7, v11, v10
	v_div_fmas_f32 v7, v7, v9, v11
	v_div_fixup_f32 v4, v7, v5, v4
	ds_write_b32 v6, v4
	v_add_u32_e32 v6, 0x800, v6
	s_waitcnt vmcnt(13)
	v_mov_b32_e32 v4, v167
	v_mul_f32_e32 v5, 0xbfb8aa3b, v4
	v_exp_f32_e32 v5, v5
	s_nop 0
	v_add_f32_e32 v5, 1.0, v5
	v_div_scale_f32 v7, s[38:39], v5, v5, v4
	v_rcp_f32_e32 v9, v7
	v_div_scale_f32 v10, vcc, v4, v5, v4
	v_fma_f32 v11, -v7, v9, 1.0
	v_fmac_f32_e32 v9, v11, v9
	v_mul_f32_e32 v11, v10, v9
	v_fma_f32 v12, -v7, v11, v10
	v_fmac_f32_e32 v11, v12, v9
	v_fma_f32 v7, -v7, v11, v10
	v_div_fmas_f32 v7, v7, v9, v11
	v_div_fixup_f32 v4, v7, v5, v4
	ds_write_b32 v6, v4
	v_add_u32_e32 v6, 0x800, v6
	s_waitcnt vmcnt(12)
	v_mov_b32_e32 v4, v168
	v_mul_f32_e32 v5, 0xbfb8aa3b, v4
	v_exp_f32_e32 v5, v5
	s_nop 0
	v_add_f32_e32 v5, 1.0, v5
	v_div_scale_f32 v7, s[38:39], v5, v5, v4
	v_rcp_f32_e32 v9, v7
	v_div_scale_f32 v10, vcc, v4, v5, v4
	v_fma_f32 v11, -v7, v9, 1.0
	v_fmac_f32_e32 v9, v11, v9
	v_mul_f32_e32 v11, v10, v9
	v_fma_f32 v12, -v7, v11, v10
	v_fmac_f32_e32 v11, v12, v9
	v_fma_f32 v7, -v7, v11, v10
	v_div_fmas_f32 v7, v7, v9, v11
	v_div_fixup_f32 v4, v7, v5, v4
	ds_write_b32 v6, v4
	v_add_u32_e32 v6, 0x800, v6
	s_waitcnt vmcnt(11)
	v_mov_b32_e32 v4, v169
	v_mul_f32_e32 v5, 0xbfb8aa3b, v4
	v_exp_f32_e32 v5, v5
	s_nop 0
	v_add_f32_e32 v5, 1.0, v5
	v_div_scale_f32 v7, s[38:39], v5, v5, v4
	v_rcp_f32_e32 v9, v7
	v_div_scale_f32 v10, vcc, v4, v5, v4
	v_fma_f32 v11, -v7, v9, 1.0
	v_fmac_f32_e32 v9, v11, v9
	v_mul_f32_e32 v11, v10, v9
	v_fma_f32 v12, -v7, v11, v10
	v_fmac_f32_e32 v11, v12, v9
	v_fma_f32 v7, -v7, v11, v10
	v_div_fmas_f32 v7, v7, v9, v11
	v_div_fixup_f32 v4, v7, v5, v4
	ds_write_b32 v6, v4
	v_add_u32_e32 v6, 0x800, v6
	s_waitcnt vmcnt(10)
	v_mov_b32_e32 v4, v170
	v_mul_f32_e32 v5, 0xbfb8aa3b, v4
	v_exp_f32_e32 v5, v5
	s_nop 0
	v_add_f32_e32 v5, 1.0, v5
	v_div_scale_f32 v7, s[38:39], v5, v5, v4
	v_rcp_f32_e32 v9, v7
	v_div_scale_f32 v10, vcc, v4, v5, v4
	v_fma_f32 v11, -v7, v9, 1.0
	v_fmac_f32_e32 v9, v11, v9
	v_mul_f32_e32 v11, v10, v9
	v_fma_f32 v12, -v7, v11, v10
	v_fmac_f32_e32 v11, v12, v9
	v_fma_f32 v7, -v7, v11, v10
	v_div_fmas_f32 v7, v7, v9, v11
	v_div_fixup_f32 v4, v7, v5, v4
	ds_write_b32 v6, v4
	v_add_u32_e32 v6, 0x800, v6
	s_waitcnt vmcnt(9)
	v_mov_b32_e32 v4, v171
	v_mul_f32_e32 v5, 0xbfb8aa3b, v4
	v_exp_f32_e32 v5, v5
	s_nop 0
	v_add_f32_e32 v5, 1.0, v5
	v_div_scale_f32 v7, s[38:39], v5, v5, v4
	v_rcp_f32_e32 v9, v7
	v_div_scale_f32 v10, vcc, v4, v5, v4
	v_fma_f32 v11, -v7, v9, 1.0
	v_fmac_f32_e32 v9, v11, v9
	v_mul_f32_e32 v11, v10, v9
	v_fma_f32 v12, -v7, v11, v10
	v_fmac_f32_e32 v11, v12, v9
	v_fma_f32 v7, -v7, v11, v10
	v_div_fmas_f32 v7, v7, v9, v11
	v_div_fixup_f32 v4, v7, v5, v4
	ds_write_b32 v6, v4
	v_add_u32_e32 v6, 0x800, v6
	s_waitcnt vmcnt(8)
	v_mov_b32_e32 v4, v172
	v_mul_f32_e32 v5, 0xbfb8aa3b, v4
	v_exp_f32_e32 v5, v5
	s_nop 0
	v_add_f32_e32 v5, 1.0, v5
	v_div_scale_f32 v7, s[38:39], v5, v5, v4
	v_rcp_f32_e32 v9, v7
	v_div_scale_f32 v10, vcc, v4, v5, v4
	v_fma_f32 v11, -v7, v9, 1.0
	v_fmac_f32_e32 v9, v11, v9
	v_mul_f32_e32 v11, v10, v9
	v_fma_f32 v12, -v7, v11, v10
	v_fmac_f32_e32 v11, v12, v9
	v_fma_f32 v7, -v7, v11, v10
	v_div_fmas_f32 v7, v7, v9, v11
	v_div_fixup_f32 v4, v7, v5, v4
	ds_write_b32 v6, v4
	v_add_u32_e32 v6, 0x800, v6
	s_waitcnt vmcnt(7)
	v_mov_b32_e32 v4, v173
	v_mul_f32_e32 v5, 0xbfb8aa3b, v4
	v_exp_f32_e32 v5, v5
	s_nop 0
	v_add_f32_e32 v5, 1.0, v5
	v_div_scale_f32 v7, s[38:39], v5, v5, v4
	v_rcp_f32_e32 v9, v7
	v_div_scale_f32 v10, vcc, v4, v5, v4
	v_fma_f32 v11, -v7, v9, 1.0
	v_fmac_f32_e32 v9, v11, v9
	v_mul_f32_e32 v11, v10, v9
	v_fma_f32 v12, -v7, v11, v10
	v_fmac_f32_e32 v11, v12, v9
	v_fma_f32 v7, -v7, v11, v10
	v_div_fmas_f32 v7, v7, v9, v11
	v_div_fixup_f32 v4, v7, v5, v4
	ds_write_b32 v6, v4
	v_add_u32_e32 v6, 0x800, v6
	s_waitcnt vmcnt(6)
	v_mov_b32_e32 v4, v174
	v_mul_f32_e32 v5, 0xbfb8aa3b, v4
	v_exp_f32_e32 v5, v5
	s_nop 0
	v_add_f32_e32 v5, 1.0, v5
	v_div_scale_f32 v7, s[38:39], v5, v5, v4
	v_rcp_f32_e32 v9, v7
	v_div_scale_f32 v10, vcc, v4, v5, v4
	v_fma_f32 v11, -v7, v9, 1.0
	v_fmac_f32_e32 v9, v11, v9
	v_mul_f32_e32 v11, v10, v9
	v_fma_f32 v12, -v7, v11, v10
	v_fmac_f32_e32 v11, v12, v9
	v_fma_f32 v7, -v7, v11, v10
	v_div_fmas_f32 v7, v7, v9, v11
	v_div_fixup_f32 v4, v7, v5, v4
	ds_write_b32 v6, v4
	v_add_u32_e32 v6, 0x800, v6
	s_waitcnt vmcnt(5)
	v_mov_b32_e32 v4, v175
	v_mul_f32_e32 v5, 0xbfb8aa3b, v4
	v_exp_f32_e32 v5, v5
	s_nop 0
	v_add_f32_e32 v5, 1.0, v5
	v_div_scale_f32 v7, s[38:39], v5, v5, v4
	v_rcp_f32_e32 v9, v7
	v_div_scale_f32 v10, vcc, v4, v5, v4
	v_fma_f32 v11, -v7, v9, 1.0
	v_fmac_f32_e32 v9, v11, v9
	v_mul_f32_e32 v11, v10, v9
	v_fma_f32 v12, -v7, v11, v10
	v_fmac_f32_e32 v11, v12, v9
	v_fma_f32 v7, -v7, v11, v10
	v_div_fmas_f32 v7, v7, v9, v11
	v_div_fixup_f32 v4, v7, v5, v4
	ds_write_b32 v6, v4
	v_add_u32_e32 v6, 0x800, v6
	s_waitcnt vmcnt(4)
	v_mov_b32_e32 v4, v176
	v_mul_f32_e32 v5, 0xbfb8aa3b, v4
	v_exp_f32_e32 v5, v5
	s_nop 0
	v_add_f32_e32 v5, 1.0, v5
	v_div_scale_f32 v7, s[38:39], v5, v5, v4
	v_rcp_f32_e32 v9, v7
	v_div_scale_f32 v10, vcc, v4, v5, v4
	v_fma_f32 v11, -v7, v9, 1.0
	v_fmac_f32_e32 v9, v11, v9
	v_mul_f32_e32 v11, v10, v9
	v_fma_f32 v12, -v7, v11, v10
	v_fmac_f32_e32 v11, v12, v9
	v_fma_f32 v7, -v7, v11, v10
	v_div_fmas_f32 v7, v7, v9, v11
	v_div_fixup_f32 v4, v7, v5, v4
	ds_write_b32 v6, v4
	v_add_u32_e32 v6, 0x800, v6
	s_waitcnt vmcnt(3)
	v_mov_b32_e32 v4, v177
	v_mul_f32_e32 v5, 0xbfb8aa3b, v4
	v_exp_f32_e32 v5, v5
	s_nop 0
	v_add_f32_e32 v5, 1.0, v5
	v_div_scale_f32 v7, s[38:39], v5, v5, v4
	v_rcp_f32_e32 v9, v7
	v_div_scale_f32 v10, vcc, v4, v5, v4
	v_fma_f32 v11, -v7, v9, 1.0
	v_fmac_f32_e32 v9, v11, v9
	v_mul_f32_e32 v11, v10, v9
	v_fma_f32 v12, -v7, v11, v10
	v_fmac_f32_e32 v11, v12, v9
	v_fma_f32 v7, -v7, v11, v10
	v_div_fmas_f32 v7, v7, v9, v11
	v_div_fixup_f32 v4, v7, v5, v4
	ds_write_b32 v6, v4
	v_add_u32_e32 v6, 0x800, v6
	s_waitcnt vmcnt(2)
	v_mov_b32_e32 v4, v178
	v_mul_f32_e32 v5, 0xbfb8aa3b, v4
	v_exp_f32_e32 v5, v5
	s_nop 0
	v_add_f32_e32 v5, 1.0, v5
	v_div_scale_f32 v7, s[38:39], v5, v5, v4
	v_rcp_f32_e32 v9, v7
	v_div_scale_f32 v10, vcc, v4, v5, v4
	v_fma_f32 v11, -v7, v9, 1.0
	v_fmac_f32_e32 v9, v11, v9
	v_mul_f32_e32 v11, v10, v9
	v_fma_f32 v12, -v7, v11, v10
	v_fmac_f32_e32 v11, v12, v9
	v_fma_f32 v7, -v7, v11, v10
	v_div_fmas_f32 v7, v7, v9, v11
	v_div_fixup_f32 v4, v7, v5, v4
	ds_write_b32 v6, v4
	v_add_u32_e32 v6, 0x800, v6
	s_waitcnt vmcnt(1)
	v_mov_b32_e32 v4, v179
	v_mul_f32_e32 v5, 0xbfb8aa3b, v4
	v_exp_f32_e32 v5, v5
	s_nop 0
	v_add_f32_e32 v5, 1.0, v5
	v_div_scale_f32 v7, s[38:39], v5, v5, v4
	v_rcp_f32_e32 v9, v7
	v_div_scale_f32 v10, vcc, v4, v5, v4
	v_fma_f32 v11, -v7, v9, 1.0
	v_fmac_f32_e32 v9, v11, v9
	v_mul_f32_e32 v11, v10, v9
	v_fma_f32 v12, -v7, v11, v10
	v_fmac_f32_e32 v11, v12, v9
	v_fma_f32 v7, -v7, v11, v10
	v_div_fmas_f32 v7, v7, v9, v11
	v_div_fixup_f32 v4, v7, v5, v4
	ds_write_b32 v6, v4
	v_add_u32_e32 v6, 0x800, v6
	s_waitcnt vmcnt(0)
	v_mov_b32_e32 v4, v180
	v_mul_f32_e32 v5, 0xbfb8aa3b, v4
	v_exp_f32_e32 v5, v5
	s_nop 0
	v_add_f32_e32 v5, 1.0, v5
	v_div_scale_f32 v7, s[38:39], v5, v5, v4
	v_rcp_f32_e32 v9, v7
	v_div_scale_f32 v10, vcc, v4, v5, v4
	v_fma_f32 v11, -v7, v9, 1.0
	v_fmac_f32_e32 v9, v11, v9
	v_mul_f32_e32 v11, v10, v9
	v_fma_f32 v12, -v7, v11, v10
	v_fmac_f32_e32 v11, v12, v9
	v_fma_f32 v7, -v7, v11, v10
	v_div_fmas_f32 v7, v7, v9, v11
	v_div_fixup_f32 v4, v7, v5, v4
	ds_write_b32 v6, v4
	v_add_u32_e32 v6, 0x800, v6
